# GEMM1 expert u-table conversion loop: next trip's two rows are loaded one trip ahead into spare registers (software pipelining)
# baseline (speedup 1.0000x reference)
; #define GAS __attribute__((address_space(1)))
; #define LAS __attribute__((address_space(3)))
; __device__ __forceinline__ void row_to_fp8_2(int lane, const float* xrow0, const float* xrow1, unsigned (&ow0)[4], unsigned (&ow1)[4], float& isc0, float& isc1) {
;     const GAS f32x4* xr0 = (const GAS f32x4*)xrow0 + lane; const GAS f32x4* xr1 = (const GAS f32x4*)xrow1 + lane;
;     f32x4 v0[4], v1[4];
; #pragma unroll
;     for (int j = 0; j < 4; ++j) { v0[j] = __builtin_nontemporal_load(xr0 + 64 * j); v1[j] = __builtin_nontemporal_load(xr1 + 64 * j); }
; __device__ __forceinline__ void tables_part(LAS unsigned char* lds, int wave, int lane, const float* pu, const float* pv, unsigned char* ws, int gw, int ngw, int wg, int nwg, int r0, int r1, int i0, int i1) {
;     for (int m = r0 + gw; m < r1; m += 2 * ngw) {
;         const int m1 = (m + ngw < r1) ? m + ngw : m;
;         float isc0, isc1; unsigned ow0[4], ow1[4];
;         row_to_fp8_2(lane, pu + (size_t)m * D, pu + (size_t)m1 * D, ow0, ow1, isc0, isc1);
.LBB0_176:
	s_cmpk_lt_i32 s3, 0x80
	s_cselect_b32 s99, 0x100, 0
	s_add_i32 s3, s3, s99
	v_xor_b32_e32 v0, 16, v172
	v_cmp_lt_i32_e32 vcc, v0, v177
	s_add_i32 s8, s3, 0xffffff80
	s_waitcnt lgkmcnt(0)
	v_xor_b32_e32 v1, 32, v172
	v_cndmask_b32_e32 v0, v172, v0, vcc
	v_lshlrev_b32_e32 v10, 2, v0
	v_mov_b32_e32 v0, v172
	s_load_dwordx2 s[14:15], s[12:13], 0x60
	s_lshl_b32 s4, s8, 3
	v_cmp_lt_i32_e32 vcc, v1, v177
	s_add_i32 s6, s4, s61
	s_cmpk_gt_i32 s6, 0x3fff
	v_cndmask_b32_e32 v1, v172, v1, vcc
	v_lshlrev_b32_e32 v11, 2, v1
	s_cbranch_scc1 .LBB0_181
	s_cmp_lg_u32 s99, 0
	s_cbranch_scc1 .LBB0_181
	v_ashrrev_i32_e32 v1, 31, v0
	s_add_u32 s9, s10, 0x19000000
	v_lshlrev_b64 v[6:7], 2, v[0:1]
	s_load_dwordx2 s[12:13], s[12:13], 0x58
	s_addc_u32 s22, s11, 0
	v_lshl_add_u64 v[4:5], s[10:11], 0, v[6:7]
	s_mov_b64 s[16:17], 0x15000000
	s_ashr_i32 s7, s6, 31
	v_lshl_add_u64 v[4:5], v[4:5], 0, s[16:17]
	s_lshl_b64 s[16:17], s[6:7], 3
	s_add_u32 s23, s16, 0x19000000
	s_addc_u32 s24, s17, 0
	s_lshl_b64 s[16:17], s[6:7], 10
	v_lshlrev_b64 v[8:9], 4, v[0:1]
	v_lshl_add_u64 v[6:7], s[16:17], 0, v[6:7]
	s_lshl_b64 s[16:17], s[6:7], 12
	s_waitcnt lgkmcnt(0)
	v_lshl_add_u64 v[2:3], s[12:13], 0, v[8:9]
	s_add_u32 s12, s12, s16
	s_addc_u32 s13, s13, s17
	v_lshl_add_u64 v[8:9], s[12:13], 0, v[8:9]
	s_mov_b64 s[12:13], 0x800
	v_cmp_eq_u32_e64 s[4:5], 0, v0
	v_lshl_add_u64 v[8:9], v[8:9], 0, s[12:13]
	v_mov_b32_e32 v1, 0xf0
	v_mov_b32_e32 v12, 0
	s_mov_b64 s[12:13], 0x200000
	s_mov_b64 s[16:17], 0x800000
	global_load_dwordx4 v[214:217], v[8:9], off offset:-2048 nt
	global_load_dwordx4 v[218:221], v[8:9], off offset:-1024 nt
	global_load_dwordx4 v[222:225], v[8:9], off nt
	global_load_dwordx4 v[226:229], v[8:9], off offset:1024 nt
	s_add_i32 s63, s6, 0x400
	s_cmpk_lt_i32 s6, 0x3c00
	s_cselect_b32 s64, s63, s6
	s_ashr_i32 s65, s64, 31
	s_lshl_b64 s[64:65], s[64:65], 12
	v_lshl_add_u64 v[210:211], v[2:3], 0, s[64:65]
	s_nop 1
	global_load_dwordx4 v[230:233], v[210:211], off nt
	global_load_dwordx4 v[234:237], v[210:211], off offset:1024 nt
	global_load_dwordx4 v[238:241], v[210:211], off offset:2048 nt
	global_load_dwordx4 v[242:245], v[210:211], off offset:3072 nt
	s_mov_b32 s101, 0
	s_branch .LBB0_179

; #define GAS __attribute__((address_space(1)))
; __device__ __forceinline__ void row_to_fp8_2(int lane, const float* xrow0, const float* xrow1, unsigned (&ow0)[4], unsigned (&ow1)[4], float& isc0, float& isc1) {
;     const GAS f32x4* xr0 = (const GAS f32x4*)xrow0 + lane; const GAS f32x4* xr1 = (const GAS f32x4*)xrow1 + lane;
;     f32x4 v0[4], v1[4];
; #pragma unroll
;     for (int j = 0; j < 4; ++j) { v0[j] = __builtin_nontemporal_load(xr0 + 64 * j); v1[j] = __builtin_nontemporal_load(xr1 + 64 * j); }
; __device__ __forceinline__ void tables_part(LAS unsigned char* lds, int wave, int lane, const float* pu, const float* pv, unsigned char* ws, int gw, int ngw, int wg, int nwg, int r0, int r1, int i0, int i1) {
;     for (int m = r0 + gw; m < r1; m += 2 * ngw) {
;         const int m1 = (m + ngw < r1) ? m + ngw : m;
;         float isc0, isc1; unsigned ow0[4], ow1[4];
;         row_to_fp8_2(lane, pu + (size_t)m * D, pu + (size_t)m1 * D, ow0, ow1, isc0, isc1);
.LBB0_179:
	s_cmp_lg_u32 s101, 0
	s_cbranch_scc1 .Lup0_w
	s_waitcnt vmcnt(0)
	s_mov_b32 s101, 1
	s_branch .Lup0_j
.Lup0_w:
	s_waitcnt vmcnt(8)
.Lup0_j:
	v_mov_b32_e32 v14, v214
	v_mov_b32_e32 v15, v215
	v_mov_b32_e32 v16, v216
	v_mov_b32_e32 v17, v217
	v_mov_b32_e32 v18, v218
	v_mov_b32_e32 v19, v219
	v_mov_b32_e32 v20, v220
	v_mov_b32_e32 v21, v221
	v_mov_b32_e32 v22, v222
	v_mov_b32_e32 v23, v223
	v_mov_b32_e32 v24, v224
	v_mov_b32_e32 v25, v225
	v_mov_b32_e32 v26, v226
	v_mov_b32_e32 v27, v227
	v_mov_b32_e32 v28, v228
	v_mov_b32_e32 v29, v229
	v_mov_b32_e32 v30, v230
	v_mov_b32_e32 v31, v231
	v_mov_b32_e32 v32, v232
	v_mov_b32_e32 v33, v233
	v_mov_b32_e32 v34, v234
	v_mov_b32_e32 v35, v235
	v_mov_b32_e32 v36, v236
	v_mov_b32_e32 v37, v237
	v_mov_b32_e32 v38, v238
	v_mov_b32_e32 v39, v239
	v_mov_b32_e32 v40, v240
	v_mov_b32_e32 v41, v241
	v_mov_b32_e32 v42, v242
	v_mov_b32_e32 v43, v243
	v_mov_b32_e32 v44, v244
	v_mov_b32_e32 v45, v245
	s_cmpk_gt_i32 s6, 0x37ff
	s_cbranch_scc1 .Lup0_nopf
	s_add_i32 s62, s6, 0x800
	v_lshl_add_u64 v[246:247], v[8:9], 0, s[16:17]
	s_nop 1
	global_load_dwordx4 v[214:217], v[246:247], off offset:-2048 nt
	global_load_dwordx4 v[218:221], v[246:247], off offset:-1024 nt
	global_load_dwordx4 v[222:225], v[246:247], off nt
	global_load_dwordx4 v[226:229], v[246:247], off offset:1024 nt
	s_add_i32 s63, s62, 0x400
	s_cmpk_lt_i32 s62, 0x3c00
	s_cselect_b32 s64, s63, s62
	s_ashr_i32 s65, s64, 31
	s_lshl_b64 s[64:65], s[64:65], 12
	v_lshl_add_u64 v[210:211], v[2:3], 0, s[64:65]
	s_nop 1
	global_load_dwordx4 v[230:233], v[210:211], off nt
	global_load_dwordx4 v[234:237], v[210:211], off offset:1024 nt
	global_load_dwordx4 v[238:241], v[210:211], off offset:2048 nt
	global_load_dwordx4 v[242:245], v[210:211], off offset:3072 nt
; #define GAS __attribute__((address_space(1)))
; __device__ __forceinline__ void row_to_fp8_2(int lane, const float* xrow0, const float* xrow1, unsigned (&ow0)[4], unsigned (&ow1)[4], float& isc0, float& isc1) {
;     ...
;     float m0 = 0.f, m1 = 0.f;
; #pragma unroll
;     for (int j = 0; j < 4; ++j) { m0 = fmaxf(m0, fmaxf(fmaxf(fabsf(v0[j].x), fabsf(v0[j].y)), fmaxf(fabsf(v0[j].z), fabsf(v0[j].w)))); m1 = fmaxf(m1, fmaxf(fmaxf(fabsf(v1[j].x), fabsf(v1[j].y)), fmaxf(fabsf(v1[j].z), fabsf(v1[j].w)))); }
; #pragma unroll
;     for (int o = 1; o < 64; o <<= 1) { m0 = fmaxf(m0, __shfl_xor(m0, o)); m1 = fmaxf(m1, __shfl_xor(m1, o)); }
;     int b0 = (int)((__float_as_uint(m0) >> 23) & 255u); b0 = b0 < 16 ? 16 : (b0 > 240 ? 240 : b0);
;     int b1 = (int)((__float_as_uint(m1) >> 23) & 255u); b1 = b1 < 16 ? 16 : (b1 > 240 ? 240 : b1);
;     const float s0 = __uint_as_float((unsigned)(261 - b0) << 23), s1 = __uint_as_float((unsigned)(261 - b1) << 23);
;     isc0 = __uint_as_float((unsigned)(b0 - 7) << 23); isc1 = __uint_as_float((unsigned)(b1 - 7) << 23);
; #pragma unroll
;     for (int j = 0; j < 4; ++j) { int p = __builtin_amdgcn_cvt_pk_fp8_f32(v0[j].x * s0, v0[j].y * s0, 0, false); p = __builtin_amdgcn_cvt_pk_fp8_f32(v0[j].z * s0, v0[j].w * s0, p, true); ow0[j] = (unsigned)p;
;         int q = __builtin_amdgcn_cvt_pk_fp8_f32(v1[j].x * s1, v1[j].y * s1, 0, false); q = __builtin_amdgcn_cvt_pk_fp8_f32(v1[j].z * s1, v1[j].w * s1, q, true); ow1[j] = (unsigned)q; }
; __device__ __forceinline__ void tables_part(LAS unsigned char* lds, int wave, int lane, const float* pu, const float* pv, unsigned char* ws, int gw, int ngw, int wg, int nwg, int r0, int r1, int i0, int i1) {
;     ...
; #pragma unroll
;         for (int j = 0; j < 4; ++j) { *((GAS unsigned*)(ws + WS_UT + (size_t)m * D + j * 256) + lane) = ow0[j]; *((GAS unsigned*)(ws + WS_UT + (size_t)m1 * D + j * 256) + lane) = ow1[j]; }
;         if (lane == 0) { ((float*)(ws + WS_ESC))[m] = isc0; ((float*)(ws + WS_ESC))[m1] = isc1; } }
.Lup0_nopf:
	s_add_i32 s7, s6, 0x400
	s_cmpk_lt_i32 s6, 0x3c00
	s_cselect_b32 s18, s7, s6
	s_ashr_i32 s19, s18, 31
	v_mov_b32_e32 v55, 0
	s_lshl_b64 s[20:21], s[18:19], 10
	v_max_f32_e64 v13, |v17|, |v17|
	v_max_f32_e64 v46, |v16|, |v16|
	v_max_f32_e64 v47, |v21|, |v21|
	v_max_f32_e64 v48, |v20|, |v20|
	v_max_f32_e64 v49, |v25|, |v25|
	v_max_f32_e64 v50, |v24|, |v24|
	v_max_f32_e64 v51, |v29|, |v29|
	v_max_f32_e64 v52, |v28|, |v28|
	v_max_f32_e32 v13, v46, v13
	v_max_f32_e32 v46, v48, v47
	v_max_f32_e32 v47, v50, v49
	v_max_f32_e32 v48, v52, v51
	v_max3_f32 v13, |v14|, |v15|, v13
	v_max3_f32 v46, |v18|, |v19|, v46
	v_max3_f32 v47, |v22|, |v23|, v47
	v_max3_f32 v48, |v26|, |v27|, v48
	v_max3_f32 v13, v13, 0, v46
	v_max3_f32 v13, v13, v47, v48
	ds_bpermute_b32 v46, v173, v13
	v_max_f32_e64 v47, |v33|, |v33|
	v_max_f32_e64 v48, |v32|, |v32|
	v_max_f32_e64 v49, |v37|, |v37|
	v_max_f32_e64 v50, |v36|, |v36|
	v_max_f32_e64 v51, |v41|, |v41|
	v_max_f32_e64 v52, |v40|, |v40|
	v_max_f32_e64 v53, |v45|, |v45|
	v_max_f32_e64 v54, |v44|, |v44|
	v_max_f32_e32 v47, v48, v47
	v_max_f32_e32 v48, v50, v49
	v_max_f32_e32 v49, v52, v51
	v_max_f32_e32 v50, v54, v53
	v_max3_f32 v47, |v30|, |v31|, v47
	v_max3_f32 v48, |v34|, |v35|, v48
	v_max3_f32 v49, |v38|, |v39|, v49
	v_max3_f32 v50, |v42|, |v43|, v50
	v_max3_f32 v47, v47, 0, v48
	v_max3_f32 v47, v47, v49, v50
	s_waitcnt lgkmcnt(0)
	v_max_f32_e32 v46, v46, v46
	ds_bpermute_b32 v48, v173, v47
	v_max_f32_e32 v13, v13, v46
	ds_bpermute_b32 v46, v174, v13
	v_mov_b32_e32 v49, 0
	v_mov_b32_e32 v53, 0
	s_waitcnt lgkmcnt(1)
	v_max_f32_e32 v48, v48, v48
	v_max_f32_e32 v47, v47, v48
	s_waitcnt lgkmcnt(0)
	v_max_f32_e32 v46, v46, v46
	ds_bpermute_b32 v48, v174, v47
	v_max_f32_e32 v13, v13, v46
	ds_bpermute_b32 v46, v175, v13
	v_mov_b32_e32 v51, 0
	v_mov_b32_e32 v54, 0
	s_waitcnt lgkmcnt(1)
	v_max_f32_e32 v48, v48, v48
	v_max_f32_e32 v47, v47, v48
	s_waitcnt lgkmcnt(0)
	v_max_f32_e32 v46, v46, v46
	ds_bpermute_b32 v48, v175, v47
	v_max_f32_e32 v13, v13, v46
	ds_bpermute_b32 v46, v176, v13
	v_mov_b32_e32 v50, 0
	v_mov_b32_e32 v52, 0
	s_waitcnt lgkmcnt(1)
	v_max_f32_e32 v48, v48, v48
	v_max_f32_e32 v47, v47, v48
	s_waitcnt lgkmcnt(0)
	v_max_f32_e32 v46, v46, v46
	ds_bpermute_b32 v48, v176, v47
	v_max_f32_e32 v13, v13, v46
	ds_bpermute_b32 v46, v10, v13
	s_waitcnt lgkmcnt(1)
	v_max_f32_e32 v48, v48, v48
	v_max_f32_e32 v47, v47, v48
	s_waitcnt lgkmcnt(0)
	v_max_f32_e32 v46, v46, v46
	ds_bpermute_b32 v48, v10, v47
	v_max_f32_e32 v13, v13, v46
	ds_bpermute_b32 v46, v11, v13
	s_waitcnt lgkmcnt(1)
	v_max_f32_e32 v48, v48, v48
	v_max_f32_e32 v47, v47, v48
	s_waitcnt lgkmcnt(0)
	v_max_f32_e32 v46, v46, v46
	v_max_f32_e32 v13, v13, v46
	ds_bpermute_b32 v46, v11, v47
	v_bfe_u32 v13, v13, 23, 8
	v_med3_u32 v13, v13, 16, v1
	v_lshlrev_b32_e32 v13, 23, v13
	v_sub_u32_e32 v48, 0x82800000, v13
	s_waitcnt lgkmcnt(0)
	v_max_f32_e32 v46, v46, v46
	v_mul_f32_e32 v14, v14, v48
	v_mul_f32_e32 v15, v15, v48
	v_mul_f32_e32 v22, v22, v48
	v_mul_f32_e32 v23, v23, v48
	v_max_f32_e32 v46, v47, v46
	v_cvt_pk_fp8_f32 v49, v14, v15
	v_cvt_pk_fp8_f32 v53, v22, v23
	v_bfe_u32 v14, v46, 23, 8
	v_med3_u32 v14, v14, 16, v1
	v_lshlrev_b32_e32 v14, 23, v14
	v_mul_f32_e32 v18, v18, v48
	v_mul_f32_e32 v19, v19, v48
	v_mul_f32_e32 v24, v24, v48
	v_mul_f32_e32 v25, v25, v48
	v_sub_u32_e32 v15, 0x82800000, v14
	v_cvt_pk_fp8_f32 v51, v18, v19
	v_cvt_pk_fp8_f32 v53, v24, v25 op_sel:[0,0,1]
	v_mul_f32_e32 v24, v38, v15
	v_mul_f32_e32 v25, v39, v15
	v_cvt_pk_fp8_f32 v54, v24, v25
	v_mul_f32_e32 v16, v16, v48
	v_mul_f32_e32 v17, v17, v48
	v_mul_f32_e32 v20, v20, v48
	v_mul_f32_e32 v21, v21, v48
	v_mul_f32_e32 v26, v26, v48
	v_mul_f32_e32 v27, v27, v48
	v_cvt_pk_fp8_f32 v49, v16, v17 op_sel:[0,0,1]
	v_mul_f32_e32 v16, v30, v15
	v_mul_f32_e32 v17, v31, v15
	v_cvt_pk_fp8_f32 v55, v26, v27
	v_cvt_pk_fp8_f32 v51, v20, v21 op_sel:[0,0,1]
	v_mul_f32_e32 v20, v34, v15
	v_mul_f32_e32 v21, v35, v15
	v_mul_f32_e32 v26, v40, v15
	v_cvt_pk_fp8_f32 v50, v16, v17
	v_mul_f32_e32 v16, v41, v15
	v_cvt_pk_fp8_f32 v52, v20, v21
	v_cvt_pk_fp8_f32 v54, v26, v16 op_sel:[0,0,1]
	v_mul_f32_e32 v16, v42, v15
	v_mul_f32_e32 v17, v43, v15
	v_mov_b32_e32 v20, 0
	v_cvt_pk_fp8_f32 v20, v16, v17
	v_mul_f32_e32 v18, v32, v15
	v_mul_f32_e32 v19, v33, v15
	v_mul_f32_e32 v22, v36, v15
	v_mul_f32_e32 v23, v37, v15
	v_cvt_pk_fp8_f32 v50, v18, v19 op_sel:[0,0,1]
	v_mul_f32_e32 v16, v44, v15
	v_mul_f32_e32 v15, v45, v15
	v_cvt_pk_fp8_f32 v20, v16, v15 op_sel:[0,0,1]
	v_lshl_add_u64 v[16:17], s[10:11], 0, v[6:7]
	v_cvt_pk_fp8_f32 v52, v22, v23 op_sel:[0,0,1]
	v_add_co_u32_e32 v16, vcc, 0x15000000, v16
	v_mul_f32_e32 v28, v28, v48
	v_mul_f32_e32 v29, v29, v48
	v_addc_co_u32_e32 v17, vcc, 0, v17, vcc
	v_lshl_add_u64 v[18:19], v[4:5], 0, s[20:21]
	v_cvt_pk_fp8_f32 v55, v28, v29 op_sel:[0,0,1]
	global_store_dword v[16:17], v49, off
	global_store_dword v[18:19], v50, off
	global_store_dword v[16:17], v51, off offset:256
	global_store_dword v[18:19], v52, off offset:256
	global_store_dword v[16:17], v53, off offset:512
	global_store_dword v[18:19], v54, off offset:512
	global_store_dword v[16:17], v55, off offset:768
	global_store_dword v[18:19], v20, off offset:768
	s_and_saveexec_b64 s[20:21], s[4:5]
	s_cbranch_execz .LBB0_178
	s_lshl_b64 s[18:19], s[18:19], 3
	s_add_u32 s18, s9, s18
	s_addc_u32 s19, s22, s19
	s_add_u32 s26, s10, s23
	v_add_u32_e32 v13, 0xfc800000, v13
	s_addc_u32 s27, s11, s24
	v_add_u32_e32 v14, 0xfc800000, v14
	global_store_dword v12, v13, s[26:27]
	global_store_dword v12, v14, s[18:19]
	s_branch .LBB0_178

; #define GAS __attribute__((address_space(1)))
; #define LAS __attribute__((address_space(3)))
; __device__ __forceinline__ void row_to_fp8_2(int lane, const float* xrow0, const float* xrow1, unsigned (&ow0)[4], unsigned (&ow1)[4], float& isc0, float& isc1) {
;     const GAS f32x4* xr0 = (const GAS f32x4*)xrow0 + lane; const GAS f32x4* xr1 = (const GAS f32x4*)xrow1 + lane;
;     f32x4 v0[4], v1[4];
; #pragma unroll
;     for (int j = 0; j < 4; ++j) { v0[j] = __builtin_nontemporal_load(xr0 + 64 * j); v1[j] = __builtin_nontemporal_load(xr1 + 64 * j); }
; __device__ __forceinline__ void tables_part(LAS unsigned char* lds, int wave, int lane, const float* pu, const float* pv, unsigned char* ws, int gw, int ngw, int wg, int nwg, int r0, int r1, int i0, int i1) {
;     for (int m = r0 + gw; m < r1; m += 2 * ngw) {
;         const int m1 = (m + ngw < r1) ? m + ngw : m;
;         float isc0, isc1; unsigned ow0[4], ow1[4];
;         row_to_fp8_2(lane, pu + (size_t)m * D, pu + (size_t)m1 * D, ow0, ow1, isc0, isc1);
.LBB0_1172:
	s_cmpk_lt_i32 s3, 0x80
	s_cselect_b32 s99, 0x100, 0
	s_add_i32 s3, s3, s99
	v_xor_b32_e32 v0, 16, v172
	v_cmp_lt_i32_e32 vcc, v0, v177
	s_lshl_b32 s4, s3, 3
	s_add_i32 s4, s61, s4
	v_cndmask_b32_e32 v0, v172, v0, vcc
	v_lshlrev_b32_e32 v10, 2, v0
	v_xor_b32_e32 v0, 32, v172
	v_cmp_lt_i32_e32 vcc, v0, v177
	s_addk_i32 s4, 0xfc00
	s_cmpk_gt_i32 s4, 0x3fff
	s_waitcnt lgkmcnt(0)
	v_cndmask_b32_e32 v1, v172, v0, vcc
	v_mov_b32_e32 v0, v172
	s_load_dwordx2 s[14:15], s[12:13], 0x60
	v_lshlrev_b32_e32 v11, 2, v1
	s_cbranch_scc1 .LBB0_1177
	s_cmp_lg_u32 s99, 0
	s_cbranch_scc1 .LBB0_1177
	s_add_u32 s20, s10, 0x19000000
	v_ashrrev_i32_e32 v1, 31, v0
	s_addc_u32 s21, s11, 0
	s_add_i32 s6, s4, 0x4000
	v_lshlrev_b64 v[6:7], 2, v[0:1]
	s_load_dwordx2 s[8:9], s[12:13], 0x58
	v_lshl_add_u64 v[4:5], s[10:11], 0, v[6:7]
	s_mov_b64 s[12:13], 0x15000000
	s_ashr_i32 s7, s6, 31
	v_lshl_add_u64 v[4:5], v[4:5], 0, s[12:13]
	s_lshl_b64 s[12:13], s[6:7], 3
	s_add_u32 s22, s12, 0x19000000
	s_addc_u32 s23, s13, 0
	s_lshl_b64 s[12:13], s[6:7], 10
	v_lshlrev_b64 v[8:9], 4, v[0:1]
	v_lshl_add_u64 v[6:7], s[12:13], 0, v[6:7]
	s_lshl_b64 s[12:13], s[6:7], 12
	s_waitcnt lgkmcnt(0)
	v_lshl_add_u64 v[2:3], s[8:9], 0, v[8:9]
	s_add_u32 s8, s8, s12
	s_addc_u32 s9, s9, s13
	v_lshl_add_u64 v[8:9], s[8:9], 0, v[8:9]
	s_mov_b64 s[8:9], 0x800
	v_cmp_eq_u32_e64 s[4:5], 0, v0
	v_lshl_add_u64 v[8:9], v[8:9], 0, s[8:9]
	v_mov_b32_e32 v1, 0xf0
	v_mov_b32_e32 v12, 0
	s_mov_b64 s[8:9], 0x200000
	s_mov_b64 s[12:13], 0x800000
	global_load_dwordx4 v[214:217], v[8:9], off offset:-2048 nt
	global_load_dwordx4 v[218:221], v[8:9], off offset:-1024 nt
	global_load_dwordx4 v[222:225], v[8:9], off nt
	global_load_dwordx4 v[226:229], v[8:9], off offset:1024 nt
	s_add_i32 s63, s6, 0x400
	s_cmpk_lt_i32 s6, 0x7c00
	s_cselect_b32 s64, s63, s6
	s_ashr_i32 s65, s64, 31
	s_lshl_b64 s[64:65], s[64:65], 12
	v_lshl_add_u64 v[210:211], v[2:3], 0, s[64:65]
	s_nop 1
	global_load_dwordx4 v[230:233], v[210:211], off nt
	global_load_dwordx4 v[234:237], v[210:211], off offset:1024 nt
	global_load_dwordx4 v[238:241], v[210:211], off offset:2048 nt
	global_load_dwordx4 v[242:245], v[210:211], off offset:3072 nt
	s_mov_b32 s101, 0
	s_branch .LBB0_1175

; #define GAS __attribute__((address_space(1)))
; __device__ __forceinline__ void row_to_fp8_2(int lane, const float* xrow0, const float* xrow1, unsigned (&ow0)[4], unsigned (&ow1)[4], float& isc0, float& isc1) {
;     const GAS f32x4* xr0 = (const GAS f32x4*)xrow0 + lane; const GAS f32x4* xr1 = (const GAS f32x4*)xrow1 + lane;
;     f32x4 v0[4], v1[4];
; #pragma unroll
;     for (int j = 0; j < 4; ++j) { v0[j] = __builtin_nontemporal_load(xr0 + 64 * j); v1[j] = __builtin_nontemporal_load(xr1 + 64 * j); }
; __device__ __forceinline__ void tables_part(LAS unsigned char* lds, int wave, int lane, const float* pu, const float* pv, unsigned char* ws, int gw, int ngw, int wg, int nwg, int r0, int r1, int i0, int i1) {
;     for (int m = r0 + gw; m < r1; m += 2 * ngw) {
;         const int m1 = (m + ngw < r1) ? m + ngw : m;
;         float isc0, isc1; unsigned ow0[4], ow1[4];
;         row_to_fp8_2(lane, pu + (size_t)m * D, pu + (size_t)m1 * D, ow0, ow1, isc0, isc1);
.Lup1_j:
	v_mov_b32_e32 v14, v214
	v_mov_b32_e32 v15, v215
	v_mov_b32_e32 v16, v216
	v_mov_b32_e32 v17, v217
	v_mov_b32_e32 v18, v218
	v_mov_b32_e32 v19, v219
	v_mov_b32_e32 v20, v220
	v_mov_b32_e32 v21, v221
	v_mov_b32_e32 v22, v222
	v_mov_b32_e32 v23, v223
	v_mov_b32_e32 v24, v224
	v_mov_b32_e32 v25, v225
	v_mov_b32_e32 v26, v226
	v_mov_b32_e32 v27, v227
	v_mov_b32_e32 v28, v228
	v_mov_b32_e32 v29, v229
	v_mov_b32_e32 v30, v230
	v_mov_b32_e32 v31, v231
	v_mov_b32_e32 v32, v232
	v_mov_b32_e32 v33, v233
	v_mov_b32_e32 v34, v234
	v_mov_b32_e32 v35, v235
	v_mov_b32_e32 v36, v236
	v_mov_b32_e32 v37, v237
	v_mov_b32_e32 v38, v238
	v_mov_b32_e32 v39, v239
	v_mov_b32_e32 v40, v240
	v_mov_b32_e32 v41, v241
	v_mov_b32_e32 v42, v242
	v_mov_b32_e32 v43, v243
	v_mov_b32_e32 v44, v244
	v_mov_b32_e32 v45, v245
	s_cmpk_gt_i32 s6, 0x77ff
	s_cbranch_scc1 .Lup1_nopf
	s_add_i32 s62, s6, 0x800
	v_lshl_add_u64 v[246:247], v[8:9], 0, s[12:13]
	s_nop 1
	global_load_dwordx4 v[214:217], v[246:247], off offset:-2048 nt
	global_load_dwordx4 v[218:221], v[246:247], off offset:-1024 nt
	global_load_dwordx4 v[222:225], v[246:247], off nt
	global_load_dwordx4 v[226:229], v[246:247], off offset:1024 nt
	s_add_i32 s63, s62, 0x400
	s_cmpk_lt_i32 s62, 0x7c00
	s_cselect_b32 s64, s63, s62
	s_ashr_i32 s65, s64, 31
	s_lshl_b64 s[64:65], s[64:65], 12
	v_lshl_add_u64 v[210:211], v[2:3], 0, s[64:65]
	s_nop 1
	global_load_dwordx4 v[230:233], v[210:211], off nt
	global_load_dwordx4 v[234:237], v[210:211], off offset:1024 nt
	global_load_dwordx4 v[238:241], v[210:211], off offset:2048 nt
	global_load_dwordx4 v[242:245], v[210:211], off offset:3072 nt
; #define GAS __attribute__((address_space(1)))
; __device__ __forceinline__ void row_to_fp8_2(int lane, const float* xrow0, const float* xrow1, unsigned (&ow0)[4], unsigned (&ow1)[4], float& isc0, float& isc1) {
;     ...
;     float m0 = 0.f, m1 = 0.f;
; #pragma unroll
;     for (int j = 0; j < 4; ++j) { m0 = fmaxf(m0, fmaxf(fmaxf(fabsf(v0[j].x), fabsf(v0[j].y)), fmaxf(fabsf(v0[j].z), fabsf(v0[j].w)))); m1 = fmaxf(m1, fmaxf(fmaxf(fabsf(v1[j].x), fabsf(v1[j].y)), fmaxf(fabsf(v1[j].z), fabsf(v1[j].w)))); }
; #pragma unroll
;     for (int o = 1; o < 64; o <<= 1) { m0 = fmaxf(m0, __shfl_xor(m0, o)); m1 = fmaxf(m1, __shfl_xor(m1, o)); }
;     int b0 = (int)((__float_as_uint(m0) >> 23) & 255u); b0 = b0 < 16 ? 16 : (b0 > 240 ? 240 : b0);
;     int b1 = (int)((__float_as_uint(m1) >> 23) & 255u); b1 = b1 < 16 ? 16 : (b1 > 240 ? 240 : b1);
;     const float s0 = __uint_as_float((unsigned)(261 - b0) << 23), s1 = __uint_as_float((unsigned)(261 - b1) << 23);
;     isc0 = __uint_as_float((unsigned)(b0 - 7) << 23); isc1 = __uint_as_float((unsigned)(b1 - 7) << 23);
; #pragma unroll
;     for (int j = 0; j < 4; ++j) { int p = __builtin_amdgcn_cvt_pk_fp8_f32(v0[j].x * s0, v0[j].y * s0, 0, false); p = __builtin_amdgcn_cvt_pk_fp8_f32(v0[j].z * s0, v0[j].w * s0, p, true); ow0[j] = (unsigned)p;
;         int q = __builtin_amdgcn_cvt_pk_fp8_f32(v1[j].x * s1, v1[j].y * s1, 0, false); q = __builtin_amdgcn_cvt_pk_fp8_f32(v1[j].z * s1, v1[j].w * s1, q, true); ow1[j] = (unsigned)q; }
; __device__ __forceinline__ void tables_part(LAS unsigned char* lds, int wave, int lane, const float* pu, const float* pv, unsigned char* ws, int gw, int ngw, int wg, int nwg, int r0, int r1, int i0, int i1) {
;     ...
; #pragma unroll
;         for (int j = 0; j < 4; ++j) { *((GAS unsigned*)(ws + WS_UT + (size_t)m * D + j * 256) + lane) = ow0[j]; *((GAS unsigned*)(ws + WS_UT + (size_t)m1 * D + j * 256) + lane) = ow1[j]; }
;         if (lane == 0) { ((float*)(ws + WS_ESC))[m] = isc0; ((float*)(ws + WS_ESC))[m1] = isc1; } }
.Lup1_nopf:
	s_add_i32 s7, s6, 0x400
	s_cmpk_lt_i32 s6, 0x7c00
	s_cselect_b32 s16, s7, s6
	s_ashr_i32 s17, s16, 31
	v_mov_b32_e32 v55, 0
	s_lshl_b64 s[18:19], s[16:17], 10
	v_max_f32_e64 v13, |v17|, |v17|
	v_max_f32_e64 v46, |v16|, |v16|
	v_max_f32_e64 v47, |v21|, |v21|
	v_max_f32_e64 v48, |v20|, |v20|
	v_max_f32_e64 v49, |v25|, |v25|
	v_max_f32_e64 v50, |v24|, |v24|
	v_max_f32_e64 v51, |v29|, |v29|
	v_max_f32_e64 v52, |v28|, |v28|
	v_max_f32_e32 v13, v46, v13
	v_max_f32_e32 v46, v48, v47
	v_max_f32_e32 v47, v50, v49
	v_max_f32_e32 v48, v52, v51
	v_max3_f32 v13, |v14|, |v15|, v13
	v_max3_f32 v46, |v18|, |v19|, v46
	v_max3_f32 v47, |v22|, |v23|, v47
	v_max3_f32 v48, |v26|, |v27|, v48
	v_max3_f32 v13, v13, 0, v46
	v_max3_f32 v13, v13, v47, v48
	ds_bpermute_b32 v46, v173, v13
	v_max_f32_e64 v47, |v33|, |v33|
	v_max_f32_e64 v48, |v32|, |v32|
	v_max_f32_e64 v49, |v37|, |v37|
	v_max_f32_e64 v50, |v36|, |v36|
	v_max_f32_e64 v51, |v41|, |v41|
	v_max_f32_e64 v52, |v40|, |v40|
	v_max_f32_e64 v53, |v45|, |v45|
	v_max_f32_e64 v54, |v44|, |v44|
	v_max_f32_e32 v47, v48, v47
	v_max_f32_e32 v48, v50, v49
	v_max_f32_e32 v49, v52, v51
	v_max_f32_e32 v50, v54, v53
	v_max3_f32 v47, |v30|, |v31|, v47
	v_max3_f32 v48, |v34|, |v35|, v48
	v_max3_f32 v49, |v38|, |v39|, v49
	v_max3_f32 v50, |v42|, |v43|, v50
	v_max3_f32 v47, v47, 0, v48
	v_max3_f32 v47, v47, v49, v50
	s_waitcnt lgkmcnt(0)
	v_max_f32_e32 v46, v46, v46
	ds_bpermute_b32 v48, v173, v47
	v_max_f32_e32 v13, v13, v46
	ds_bpermute_b32 v46, v174, v13
	v_mov_b32_e32 v49, 0
	v_mov_b32_e32 v53, 0
	s_waitcnt lgkmcnt(1)
	v_max_f32_e32 v48, v48, v48
	v_max_f32_e32 v47, v47, v48
	s_waitcnt lgkmcnt(0)
	v_max_f32_e32 v46, v46, v46
	ds_bpermute_b32 v48, v174, v47
	v_max_f32_e32 v13, v13, v46
	ds_bpermute_b32 v46, v175, v13
	v_mov_b32_e32 v51, 0
	v_mov_b32_e32 v54, 0
	s_waitcnt lgkmcnt(1)
	v_max_f32_e32 v48, v48, v48
	v_max_f32_e32 v47, v47, v48
	s_waitcnt lgkmcnt(0)
	v_max_f32_e32 v46, v46, v46
	ds_bpermute_b32 v48, v175, v47
	v_max_f32_e32 v13, v13, v46
	ds_bpermute_b32 v46, v176, v13
	v_mov_b32_e32 v50, 0
	v_mov_b32_e32 v52, 0
	s_waitcnt lgkmcnt(1)
	v_max_f32_e32 v48, v48, v48
	v_max_f32_e32 v47, v47, v48
	s_waitcnt lgkmcnt(0)
	v_max_f32_e32 v46, v46, v46
	ds_bpermute_b32 v48, v176, v47
	v_max_f32_e32 v13, v13, v46
	ds_bpermute_b32 v46, v10, v13
	s_waitcnt lgkmcnt(1)
	v_max_f32_e32 v48, v48, v48
	v_max_f32_e32 v47, v47, v48
	s_waitcnt lgkmcnt(0)
	v_max_f32_e32 v46, v46, v46
	ds_bpermute_b32 v48, v10, v47
	v_max_f32_e32 v13, v13, v46
	ds_bpermute_b32 v46, v11, v13
	s_waitcnt lgkmcnt(1)
	v_max_f32_e32 v48, v48, v48
	v_max_f32_e32 v47, v47, v48
	s_waitcnt lgkmcnt(0)
	v_max_f32_e32 v46, v46, v46
	v_max_f32_e32 v13, v13, v46
	ds_bpermute_b32 v46, v11, v47
	v_bfe_u32 v13, v13, 23, 8
	v_med3_u32 v13, v13, 16, v1
	v_lshlrev_b32_e32 v13, 23, v13
	v_sub_u32_e32 v48, 0x82800000, v13
	s_waitcnt lgkmcnt(0)
	v_max_f32_e32 v46, v46, v46
	v_mul_f32_e32 v14, v14, v48
	v_mul_f32_e32 v15, v15, v48
	v_mul_f32_e32 v22, v22, v48
	v_mul_f32_e32 v23, v23, v48
	v_max_f32_e32 v46, v47, v46
	v_cvt_pk_fp8_f32 v49, v14, v15
	v_cvt_pk_fp8_f32 v53, v22, v23
	v_bfe_u32 v14, v46, 23, 8
	v_med3_u32 v14, v14, 16, v1
	v_lshlrev_b32_e32 v14, 23, v14
	v_mul_f32_e32 v18, v18, v48
	v_mul_f32_e32 v19, v19, v48
	v_mul_f32_e32 v24, v24, v48
	v_mul_f32_e32 v25, v25, v48
	v_sub_u32_e32 v15, 0x82800000, v14
	v_cvt_pk_fp8_f32 v51, v18, v19
	v_cvt_pk_fp8_f32 v53, v24, v25 op_sel:[0,0,1]
	v_mul_f32_e32 v24, v38, v15
	v_mul_f32_e32 v25, v39, v15
	v_cvt_pk_fp8_f32 v54, v24, v25
	v_mul_f32_e32 v16, v16, v48
	v_mul_f32_e32 v17, v17, v48
	v_mul_f32_e32 v20, v20, v48
	v_mul_f32_e32 v21, v21, v48
	v_mul_f32_e32 v26, v26, v48
	v_mul_f32_e32 v27, v27, v48
	v_cvt_pk_fp8_f32 v49, v16, v17 op_sel:[0,0,1]
	v_mul_f32_e32 v16, v30, v15
	v_mul_f32_e32 v17, v31, v15
	v_cvt_pk_fp8_f32 v55, v26, v27
	v_cvt_pk_fp8_f32 v51, v20, v21 op_sel:[0,0,1]
	v_mul_f32_e32 v20, v34, v15
	v_mul_f32_e32 v21, v35, v15
	v_mul_f32_e32 v26, v40, v15
	v_cvt_pk_fp8_f32 v50, v16, v17
	v_mul_f32_e32 v16, v41, v15
	v_cvt_pk_fp8_f32 v52, v20, v21
	v_cvt_pk_fp8_f32 v54, v26, v16 op_sel:[0,0,1]
	v_mul_f32_e32 v16, v42, v15
	v_mul_f32_e32 v17, v43, v15
	v_mov_b32_e32 v20, 0
	v_cvt_pk_fp8_f32 v20, v16, v17
	v_mul_f32_e32 v18, v32, v15
	v_mul_f32_e32 v19, v33, v15
	v_mul_f32_e32 v22, v36, v15
	v_mul_f32_e32 v23, v37, v15
	v_cvt_pk_fp8_f32 v50, v18, v19 op_sel:[0,0,1]
	v_mul_f32_e32 v16, v44, v15
	v_mul_f32_e32 v15, v45, v15
	v_cvt_pk_fp8_f32 v20, v16, v15 op_sel:[0,0,1]
	v_lshl_add_u64 v[16:17], s[10:11], 0, v[6:7]
	v_cvt_pk_fp8_f32 v52, v22, v23 op_sel:[0,0,1]
	v_add_co_u32_e32 v16, vcc, 0x15000000, v16
	v_mul_f32_e32 v28, v28, v48
	v_mul_f32_e32 v29, v29, v48
	v_addc_co_u32_e32 v17, vcc, 0, v17, vcc
	v_lshl_add_u64 v[18:19], v[4:5], 0, s[18:19]
	v_cvt_pk_fp8_f32 v55, v28, v29 op_sel:[0,0,1]
	global_store_dword v[16:17], v49, off
	global_store_dword v[18:19], v50, off
	global_store_dword v[16:17], v51, off offset:256
	global_store_dword v[18:19], v52, off offset:256
	global_store_dword v[16:17], v53, off offset:512
	global_store_dword v[18:19], v54, off offset:512
	global_store_dword v[16:17], v55, off offset:768
	global_store_dword v[18:19], v20, off offset:768
	s_and_saveexec_b64 s[18:19], s[4:5]
	s_cbranch_execz .LBB0_1174
	s_lshl_b64 s[16:17], s[16:17], 3
	s_add_u32 s16, s20, s16
	s_addc_u32 s17, s21, s17
	s_add_u32 s24, s10, s22
	v_add_u32_e32 v13, 0xfc800000, v13
	s_addc_u32 s25, s11, s23
	v_add_u32_e32 v14, 0xfc800000, v14
	global_store_dword v12, v13, s[24:25]
	global_store_dword v12, v14, s[16:17]
	s_branch .LBB0_1174
